# P0 weight transposition: both 16-load batches of an item issued before the first LDS write (software pipelining, 2x loads in flight)
# speedup vs baseline: 1.3161x; 1.0044x over previous
.LBB0_25:
	s_lshl_b32 s31, s23, 1
	s_lshl_b32 s34, s4, 1
	v_or_b32_e32 v13, s31, v5
	v_or_b32_e32 v16, s34, v4
	s_add_i32 s35, s31, 4
	s_add_i32 s39, s34, 4
	s_add_i32 s42, s31, 8
	s_add_i32 s43, s34, 8
	s_add_i32 s44, s31, 12
	s_add_i32 s45, s34, 12
	s_add_i32 s46, s31, 16
	s_add_i32 s47, s34, 16
	s_add_i32 s48, s31, 20
	s_add_i32 s49, s34, 20
	s_add_i32 s50, s31, 24
	s_add_i32 s51, s34, 24
	s_add_i32 s52, s31, 28
	s_add_i32 s53, s34, 28
	v_mad_i64_i32 v[14:15], s[40:41], s19, v13, 0
	v_mad_i64_i32 v[16:17], s[40:41], s29, v16, 0
	v_or_b32_e32 v13, s35, v5
	v_or_b32_e32 v24, s39, v4
	v_or_b32_e32 v26, s42, v5
	v_or_b32_e32 v28, s43, v4
	s_waitcnt vmcnt(8)
	v_or_b32_e32 v30, s44, v5
	v_or_b32_e32 v32, s45, v4
	v_or_b32_e32 v34, s46, v5
	v_or_b32_e32 v36, s47, v4
	v_or_b32_e32 v38, s48, v5
	v_or_b32_e32 v40, s49, v4
	v_or_b32_e32 v42, s50, v5
	v_or_b32_e32 v44, s51, v4
	v_or_b32_e32 v46, s52, v5
	v_or_b32_e32 v48, s53, v4
	v_lshl_add_u64 v[16:17], v[16:17], 2, v[2:3]
	v_mad_i64_i32 v[22:23], s[40:41], s19, v13, 0
	v_mad_i64_i32 v[24:25], s[40:41], s29, v24, 0
	v_mad_i64_i32 v[26:27], s[40:41], s19, v26, 0
	v_mad_i64_i32 v[28:29], s[40:41], s29, v28, 0
	v_mad_i64_i32 v[30:31], s[40:41], s19, v30, 0
	v_mad_i64_i32 v[32:33], s[40:41], s29, v32, 0
	v_mad_i64_i32 v[34:35], s[40:41], s19, v34, 0
	v_mad_i64_i32 v[36:37], s[40:41], s29, v36, 0
	v_mad_i64_i32 v[38:39], s[40:41], s19, v38, 0
	v_mad_i64_i32 v[40:41], s[40:41], s29, v40, 0
	v_mad_i64_i32 v[42:43], s[40:41], s19, v42, 0
	v_mad_i64_i32 v[44:45], s[40:41], s29, v44, 0
	v_mad_i64_i32 v[46:47], s[40:41], s19, v46, 0
	v_mad_i64_i32 v[48:49], s[40:41], s29, v48, 0
	v_lshl_add_u64 v[14:15], v[14:15], 2, v[2:3]
	v_lshl_add_u64 v[24:25], v[24:25], 2, v[2:3]
	v_lshl_add_u64 v[22:23], v[22:23], 2, v[2:3]
	v_lshl_add_u64 v[28:29], v[28:29], 2, v[2:3]
	v_lshl_add_u64 v[26:27], v[26:27], 2, v[2:3]
	v_lshl_add_u64 v[32:33], v[32:33], 2, v[2:3]
	v_lshl_add_u64 v[30:31], v[30:31], 2, v[2:3]
	v_lshl_add_u64 v[36:37], v[36:37], 2, v[2:3]
	v_lshl_add_u64 v[34:35], v[34:35], 2, v[2:3]
	v_lshl_add_u64 v[40:41], v[40:41], 2, v[2:3]
	v_lshl_add_u64 v[38:39], v[38:39], 2, v[2:3]
	v_lshl_add_u64 v[44:45], v[44:45], 2, v[2:3]
	v_lshl_add_u64 v[42:43], v[42:43], 2, v[2:3]
	v_lshl_add_u64 v[48:49], v[48:49], 2, v[2:3]
	v_lshl_add_u64 v[46:47], v[46:47], 2, v[2:3]
	global_load_dword v13, v[16:17], off
	global_load_dword v50, v[14:15], off
	global_load_dword v51, v[24:25], off
	global_load_dword v52, v[22:23], off
	global_load_dword v53, v[28:29], off
	global_load_dword v54, v[26:27], off
	global_load_dword v55, v[32:33], off
	global_load_dword v56, v[30:31], off
	global_load_dword v57, v[36:37], off
	global_load_dword v58, v[34:35], off
	global_load_dword v59, v[40:41], off
	global_load_dword v60, v[38:39], off
	global_load_dword v61, v[44:45], off
	global_load_dword v62, v[42:43], off
	global_load_dword v63, v[48:49], off
	global_load_dword v64, v[46:47], off
	v_or_b32_e32 v16, s31, v1
	v_or_b32_e32 v14, s34, v6
	s_add_i32 s4, s4, 16
	s_add_i32 s23, s23, 16
	s_add_i32 s30, s30, -16
	v_mad_u64_u32 v[14:15], s[40:41], v14, s13, v[10:11]
	v_mad_u64_u32 v[16:17], s[40:41], v16, s13, v[10:11]
	v_or_b32_e32 v15, s35, v1
	v_or_b32_e32 v17, s39, v6
	v_or_b32_e32 v28, s42, v1
	v_or_b32_e32 v26, s43, v6
	v_or_b32_e32 v32, s44, v1
	v_or_b32_e32 v30, s45, v6
	v_or_b32_e32 v36, s46, v1
	v_or_b32_e32 v34, s47, v6
	v_or_b32_e32 v40, s48, v1
	v_or_b32_e32 v38, s49, v6
	v_or_b32_e32 v44, s50, v1
	v_or_b32_e32 v42, s51, v6
	v_or_b32_e32 v48, s52, v1
	v_or_b32_e32 v46, s53, v6
	s_cmp_lg_u32 s30, 0
	v_mad_u64_u32 v[22:23], s[34:35], v17, s13, v[10:11]
	v_mad_u64_u32 v[24:25], s[34:35], v15, s13, v[10:11]
	v_mad_u64_u32 v[26:27], s[34:35], v26, s13, v[10:11]
	v_mad_u64_u32 v[28:29], s[34:35], v28, s13, v[10:11]
	v_mad_u64_u32 v[30:31], s[34:35], v30, s13, v[10:11]
	v_mad_u64_u32 v[32:33], s[34:35], v32, s13, v[10:11]
	v_mad_u64_u32 v[34:35], s[34:35], v34, s13, v[10:11]
	v_mad_u64_u32 v[36:37], s[34:35], v36, s13, v[10:11]
	v_mad_u64_u32 v[38:39], s[34:35], v38, s13, v[10:11]
	v_mad_u64_u32 v[40:41], s[34:35], v40, s13, v[10:11]
	v_mad_u64_u32 v[42:43], s[34:35], v42, s13, v[10:11]
	v_mad_u64_u32 v[44:45], s[34:35], v44, s13, v[10:11]
	v_mad_u64_u32 v[46:47], s[34:35], v46, s13, v[10:11]
	v_mad_u64_u32 v[48:49], s[34:35], v48, s13, v[10:11]
	s_lshl_b32 s31, s23, 1
	s_lshl_b32 s34, s4, 1
	v_or_b32_e32 v77, s31, v5
	v_or_b32_e32 v80, s34, v4
	s_add_i32 s35, s31, 4
	s_add_i32 s39, s34, 4
	s_add_i32 s42, s31, 8
	s_add_i32 s43, s34, 8
	s_add_i32 s44, s31, 12
	s_add_i32 s45, s34, 12
	s_add_i32 s46, s31, 16
	s_add_i32 s47, s34, 16
	s_add_i32 s48, s31, 20
	s_add_i32 s49, s34, 20
	s_add_i32 s50, s31, 24
	s_add_i32 s51, s34, 24
	s_add_i32 s52, s31, 28
	s_add_i32 s53, s34, 28
	v_mad_i64_i32 v[78:79], s[40:41], s19, v77, 0
	v_mad_i64_i32 v[80:81], s[40:41], s29, v80, 0
	v_or_b32_e32 v77, s35, v5
	v_or_b32_e32 v88, s39, v4
	v_or_b32_e32 v90, s42, v5
	v_or_b32_e32 v92, s43, v4
	v_or_b32_e32 v94, s44, v5
	v_or_b32_e32 v96, s45, v4
	v_or_b32_e32 v98, s46, v5
	v_or_b32_e32 v100, s47, v4
	v_or_b32_e32 v102, s48, v5
	v_or_b32_e32 v104, s49, v4
	v_or_b32_e32 v106, s50, v5
	v_or_b32_e32 v108, s51, v4
	v_or_b32_e32 v110, s52, v5
	v_or_b32_e32 v112, s53, v4
	v_lshl_add_u64 v[80:81], v[80:81], 2, v[2:3]
	v_mad_i64_i32 v[86:87], s[40:41], s19, v77, 0
	v_mad_i64_i32 v[88:89], s[40:41], s29, v88, 0
	v_mad_i64_i32 v[90:91], s[40:41], s19, v90, 0
	v_mad_i64_i32 v[92:93], s[40:41], s29, v92, 0
	v_mad_i64_i32 v[94:95], s[40:41], s19, v94, 0
	v_mad_i64_i32 v[96:97], s[40:41], s29, v96, 0
	v_mad_i64_i32 v[98:99], s[40:41], s19, v98, 0
	v_mad_i64_i32 v[100:101], s[40:41], s29, v100, 0
	v_mad_i64_i32 v[102:103], s[40:41], s19, v102, 0
	v_mad_i64_i32 v[104:105], s[40:41], s29, v104, 0
	v_mad_i64_i32 v[106:107], s[40:41], s19, v106, 0
	v_mad_i64_i32 v[108:109], s[40:41], s29, v108, 0
	v_mad_i64_i32 v[110:111], s[40:41], s19, v110, 0
	v_mad_i64_i32 v[112:113], s[40:41], s29, v112, 0
	v_lshl_add_u64 v[78:79], v[78:79], 2, v[2:3]
	v_lshl_add_u64 v[88:89], v[88:89], 2, v[2:3]
	v_lshl_add_u64 v[86:87], v[86:87], 2, v[2:3]
	v_lshl_add_u64 v[92:93], v[92:93], 2, v[2:3]
	v_lshl_add_u64 v[90:91], v[90:91], 2, v[2:3]
	v_lshl_add_u64 v[96:97], v[96:97], 2, v[2:3]
	v_lshl_add_u64 v[94:95], v[94:95], 2, v[2:3]
	v_lshl_add_u64 v[100:101], v[100:101], 2, v[2:3]
	v_lshl_add_u64 v[98:99], v[98:99], 2, v[2:3]
	v_lshl_add_u64 v[104:105], v[104:105], 2, v[2:3]
	v_lshl_add_u64 v[102:103], v[102:103], 2, v[2:3]
	v_lshl_add_u64 v[108:109], v[108:109], 2, v[2:3]
	v_lshl_add_u64 v[106:107], v[106:107], 2, v[2:3]
	v_lshl_add_u64 v[112:113], v[112:113], 2, v[2:3]
	v_lshl_add_u64 v[110:111], v[110:111], 2, v[2:3]
	global_load_dword v77, v[80:81], off
	global_load_dword v114, v[78:79], off
	global_load_dword v115, v[88:89], off
	global_load_dword v116, v[86:87], off
	global_load_dword v117, v[92:93], off
	global_load_dword v118, v[90:91], off
	global_load_dword v119, v[96:97], off
	global_load_dword v120, v[94:95], off
	global_load_dword v121, v[100:101], off
	global_load_dword v122, v[98:99], off
	global_load_dword v123, v[104:105], off
	global_load_dword v124, v[102:103], off
	global_load_dword v125, v[108:109], off
	global_load_dword v126, v[106:107], off
	global_load_dword v127, v[112:113], off
	global_load_dword v128, v[110:111], off
	v_or_b32_e32 v80, s31, v1
	v_or_b32_e32 v78, s34, v6
	s_add_i32 s4, s4, 16
	s_add_i32 s23, s23, 16
	s_add_i32 s30, s30, -16
	v_mad_u64_u32 v[78:79], s[40:41], v78, s13, v[10:11]
	v_mad_u64_u32 v[80:81], s[40:41], v80, s13, v[10:11]
	v_or_b32_e32 v79, s35, v1
	v_or_b32_e32 v81, s39, v6
	v_or_b32_e32 v92, s42, v1
	v_or_b32_e32 v90, s43, v6
	v_or_b32_e32 v96, s44, v1
	v_or_b32_e32 v94, s45, v6
	v_or_b32_e32 v100, s46, v1
	v_or_b32_e32 v98, s47, v6
	v_or_b32_e32 v104, s48, v1
	v_or_b32_e32 v102, s49, v6
	v_or_b32_e32 v108, s50, v1
	v_or_b32_e32 v106, s51, v6
	v_or_b32_e32 v112, s52, v1
	v_or_b32_e32 v110, s53, v6
	s_cmp_lg_u32 s30, 0
	v_mad_u64_u32 v[86:87], s[34:35], v81, s13, v[10:11]
	v_mad_u64_u32 v[88:89], s[34:35], v79, s13, v[10:11]
	v_mad_u64_u32 v[90:91], s[34:35], v90, s13, v[10:11]
	v_mad_u64_u32 v[92:93], s[34:35], v92, s13, v[10:11]
	v_mad_u64_u32 v[94:95], s[34:35], v94, s13, v[10:11]
	v_mad_u64_u32 v[96:97], s[34:35], v96, s13, v[10:11]
	v_mad_u64_u32 v[98:99], s[34:35], v98, s13, v[10:11]
	v_mad_u64_u32 v[100:101], s[34:35], v100, s13, v[10:11]
	v_mad_u64_u32 v[102:103], s[34:35], v102, s13, v[10:11]
	v_mad_u64_u32 v[104:105], s[34:35], v104, s13, v[10:11]
	v_mad_u64_u32 v[106:107], s[34:35], v106, s13, v[10:11]
	v_mad_u64_u32 v[108:109], s[34:35], v108, s13, v[10:11]
	v_mad_u64_u32 v[110:111], s[34:35], v110, s13, v[10:11]
	v_mad_u64_u32 v[112:113], s[34:35], v112, s13, v[10:11]
	s_waitcnt vmcnt(31)
	ds_write_b32 v14, v13
	s_waitcnt vmcnt(30)
	ds_write_b32 v16, v50
	s_waitcnt vmcnt(29)
	ds_write_b32 v22, v51
	s_waitcnt vmcnt(28)
	ds_write_b32 v24, v52
	s_waitcnt vmcnt(27)
	ds_write_b32 v26, v53
	s_waitcnt vmcnt(26)
	ds_write_b32 v28, v54
	s_waitcnt vmcnt(25)
	ds_write_b32 v30, v55
	s_waitcnt vmcnt(24)
	ds_write_b32 v32, v56
	s_waitcnt vmcnt(23)
	ds_write_b32 v34, v57
	s_waitcnt vmcnt(22)
	ds_write_b32 v36, v58
	s_waitcnt vmcnt(21)
	ds_write_b32 v38, v59
	s_waitcnt vmcnt(20)
	ds_write_b32 v40, v60
	s_waitcnt vmcnt(19)
	ds_write_b32 v42, v61
	s_waitcnt vmcnt(18)
	ds_write_b32 v44, v62
	s_waitcnt vmcnt(17)
	ds_write_b32 v46, v63
	s_waitcnt vmcnt(16)
	ds_write_b32 v48, v64
	s_waitcnt vmcnt(15)
	ds_write_b32 v78, v77
	s_waitcnt vmcnt(14)
	ds_write_b32 v80, v114
	s_waitcnt vmcnt(13)
	ds_write_b32 v86, v115
	s_waitcnt vmcnt(12)
	ds_write_b32 v88, v116
	s_waitcnt vmcnt(11)
	ds_write_b32 v90, v117
	s_waitcnt vmcnt(10)
	ds_write_b32 v92, v118
	s_waitcnt vmcnt(9)
	ds_write_b32 v94, v119
	s_waitcnt vmcnt(8)
	ds_write_b32 v96, v120
	s_waitcnt vmcnt(7)
	ds_write_b32 v98, v121
	s_waitcnt vmcnt(6)
	ds_write_b32 v100, v122
	s_waitcnt vmcnt(5)
	ds_write_b32 v102, v123
	s_waitcnt vmcnt(4)
	ds_write_b32 v104, v124
	s_waitcnt vmcnt(3)
	ds_write_b32 v106, v125
	s_waitcnt vmcnt(2)
	ds_write_b32 v108, v126
	s_waitcnt vmcnt(1)
	ds_write_b32 v110, v127
	s_waitcnt vmcnt(0)
	ds_write_b32 v112, v128
	s_add_u32 s4, s24, s16
	s_addc_u32 s19, s25, s17
	s_waitcnt lgkmcnt(0)
	s_ashr_i32 s23, s22, 31
	s_lshl_b64 s[22:23], s[22:23], 1
	ds_read2_b32 v[14:15], v11 offset0:33 offset1:41
	ds_read2_b32 v[16:17], v11 offset1:8
	ds_read2_b32 v[22:23], v11 offset0:66 offset1:74
	ds_read2_b32 v[24:25], v11 offset0:99 offset1:107
	ds_read2_b32 v[26:27], v11 offset0:132 offset1:140
	ds_read2_b32 v[28:29], v11 offset0:165 offset1:173
	ds_read2_b32 v[30:31], v11 offset0:198 offset1:206
	ds_read2_b32 v[32:33], v11 offset0:231 offset1:239
	s_add_u32 s22, s4, s22
	v_or_b32_e32 v36, s18, v7
	s_addc_u32 s23, s19, s23
	v_ashrrev_i32_e32 v37, 31, v36
	v_lshl_add_u64 v[34:35], s[22:23], 0, v[8:9]
	v_lshlrev_b64 v[36:37], 12, v[36:37]
	s_waitcnt lgkmcnt(6)
	v_cvt_pk_bf16_f32 v2, v16, v14
	v_lshl_add_u64 v[36:37], v[34:35], 0, v[36:37]
	v_or_b32_e32 v14, s18, v18
	s_waitcnt lgkmcnt(4)
	v_cvt_pk_bf16_f32 v3, v22, v24
	s_waitcnt lgkmcnt(2)
	v_cvt_pk_bf16_f32 v4, v26, v28
	s_waitcnt lgkmcnt(0)
	v_cvt_pk_bf16_f32 v5, v30, v32
	global_store_dwordx4 v[36:37], v[2:5], off
	s_nop 1
	v_cvt_pk_bf16_f32 v2, v17, v15
	v_ashrrev_i32_e32 v15, 31, v14
	v_lshlrev_b64 v[14:15], 12, v[14:15]
	v_cvt_pk_bf16_f32 v3, v23, v25
	v_cvt_pk_bf16_f32 v4, v27, v29
	v_cvt_pk_bf16_f32 v5, v31, v33
	v_lshl_add_u64 v[14:15], v[34:35], 0, v[14:15]
	ds_read2_b32 v[16:17], v11 offset0:16 offset1:24
	ds_read2_b32 v[22:23], v11 offset0:49 offset1:57
	ds_read2_b32 v[24:25], v11 offset0:82 offset1:90
	ds_read2_b32 v[26:27], v11 offset0:115 offset1:123
	ds_read2_b32 v[28:29], v11 offset0:148 offset1:156
	ds_read2_b32 v[30:31], v11 offset0:181 offset1:189
	ds_read2_b32 v[32:33], v11 offset0:214 offset1:222
	ds_read2_b32 v[36:37], v11 offset0:247 offset1:255
	global_store_dwordx4 v[14:15], v[2:5], off
	v_or_b32_e32 v14, s18, v19
	v_ashrrev_i32_e32 v15, 31, v14
	v_lshlrev_b64 v[14:15], 12, v[14:15]
	v_lshl_add_u64 v[14:15], v[34:35], 0, v[14:15]
	s_waitcnt lgkmcnt(6)
	v_cvt_pk_bf16_f32 v2, v16, v22
	s_waitcnt lgkmcnt(4)
	v_cvt_pk_bf16_f32 v3, v24, v26
	s_waitcnt lgkmcnt(2)
	v_cvt_pk_bf16_f32 v4, v28, v30
	s_waitcnt lgkmcnt(0)
	v_cvt_pk_bf16_f32 v5, v32, v36
	global_store_dwordx4 v[14:15], v[2:5], off
	v_or_b32_e32 v14, s18, v20
	v_ashrrev_i32_e32 v15, 31, v14
	v_lshlrev_b64 v[14:15], 12, v[14:15]
	v_lshl_add_u64 v[14:15], v[34:35], 0, v[14:15]
	v_cvt_pk_bf16_f32 v2, v17, v23
	v_cvt_pk_bf16_f32 v3, v25, v27
	v_cvt_pk_bf16_f32 v4, v29, v31
	v_cvt_pk_bf16_f32 v5, v33, v37
	global_store_dwordx4 v[14:15], v[2:5], off
	s_waitcnt lgkmcnt(0)
	s_branch .LBB0_19

.LBB0_28:
	s_lshl_b32 s21, s4, 1
	s_lshl_b32 s28, s19, 1
	v_or_b32_e32 v16, s28, v4
	s_add_i32 s29, s21, 4
	s_add_i32 s30, s28, 4
	s_add_i32 s31, s21, 8
	s_add_i32 s34, s28, 8
	s_add_i32 s35, s21, 12
	s_add_i32 s39, s28, 12
	s_add_i32 s42, s21, 16
	s_add_i32 s43, s28, 16
	s_add_i32 s44, s21, 20
	s_add_i32 s45, s28, 20
	s_add_i32 s46, s21, 24
	s_add_i32 s47, s28, 24
	s_add_i32 s48, s21, 28
	s_add_i32 s49, s28, 28
	v_or_b32_e32 v14, s21, v5
	v_ashrrev_i32_e32 v17, 31, v16
	v_or_b32_e32 v22, s29, v5
	v_or_b32_e32 v24, s30, v4
	v_or_b32_e32 v26, s31, v5
	v_or_b32_e32 v28, s34, v4
	s_waitcnt vmcnt(8)
	v_or_b32_e32 v30, s35, v5
	v_or_b32_e32 v32, s39, v4
	v_or_b32_e32 v34, s42, v5
	v_or_b32_e32 v36, s43, v4
	v_or_b32_e32 v38, s44, v5
	v_or_b32_e32 v40, s45, v4
	v_or_b32_e32 v42, s46, v5
	v_or_b32_e32 v44, s47, v4
	v_or_b32_e32 v46, s48, v5
	v_or_b32_e32 v48, s49, v4
	v_ashrrev_i32_e32 v15, 31, v14
	v_lshlrev_b64 v[16:17], 16, v[16:17]
	v_ashrrev_i32_e32 v25, 31, v24
	v_ashrrev_i32_e32 v23, 31, v22
	v_ashrrev_i32_e32 v29, 31, v28
	v_ashrrev_i32_e32 v27, 31, v26
	v_ashrrev_i32_e32 v33, 31, v32
	v_ashrrev_i32_e32 v31, 31, v30
	v_ashrrev_i32_e32 v37, 31, v36
	v_ashrrev_i32_e32 v35, 31, v34
	v_ashrrev_i32_e32 v41, 31, v40
	v_ashrrev_i32_e32 v39, 31, v38
	v_ashrrev_i32_e32 v45, 31, v44
	v_ashrrev_i32_e32 v43, 31, v42
	v_ashrrev_i32_e32 v49, 31, v48
	v_ashrrev_i32_e32 v47, 31, v46
	v_lshlrev_b64 v[14:15], 16, v[14:15]
	v_lshl_add_u64 v[16:17], v[2:3], 0, v[16:17]
	v_lshlrev_b64 v[22:23], 16, v[22:23]
	v_lshlrev_b64 v[24:25], 16, v[24:25]
	v_lshlrev_b64 v[26:27], 16, v[26:27]
	v_lshlrev_b64 v[28:29], 16, v[28:29]
	v_lshlrev_b64 v[30:31], 16, v[30:31]
	v_lshlrev_b64 v[32:33], 16, v[32:33]
	v_lshlrev_b64 v[34:35], 16, v[34:35]
	v_lshlrev_b64 v[36:37], 16, v[36:37]
	v_lshlrev_b64 v[38:39], 16, v[38:39]
	v_lshlrev_b64 v[40:41], 16, v[40:41]
	v_lshlrev_b64 v[42:43], 16, v[42:43]
	v_lshlrev_b64 v[44:45], 16, v[44:45]
	v_lshlrev_b64 v[46:47], 16, v[46:47]
	v_lshlrev_b64 v[48:49], 16, v[48:49]
	v_lshl_add_u64 v[14:15], v[2:3], 0, v[14:15]
	v_lshl_add_u64 v[24:25], v[2:3], 0, v[24:25]
	v_lshl_add_u64 v[22:23], v[2:3], 0, v[22:23]
	v_lshl_add_u64 v[28:29], v[2:3], 0, v[28:29]
	v_lshl_add_u64 v[26:27], v[2:3], 0, v[26:27]
	v_lshl_add_u64 v[32:33], v[2:3], 0, v[32:33]
	v_lshl_add_u64 v[30:31], v[2:3], 0, v[30:31]
	v_lshl_add_u64 v[36:37], v[2:3], 0, v[36:37]
	v_lshl_add_u64 v[34:35], v[2:3], 0, v[34:35]
	v_lshl_add_u64 v[40:41], v[2:3], 0, v[40:41]
	v_lshl_add_u64 v[38:39], v[2:3], 0, v[38:39]
	v_lshl_add_u64 v[44:45], v[2:3], 0, v[44:45]
	v_lshl_add_u64 v[42:43], v[2:3], 0, v[42:43]
	v_lshl_add_u64 v[48:49], v[2:3], 0, v[48:49]
	v_lshl_add_u64 v[46:47], v[2:3], 0, v[46:47]
	global_load_dword v13, v[16:17], off
	global_load_dword v50, v[14:15], off
	global_load_dword v51, v[24:25], off
	global_load_dword v52, v[22:23], off
	global_load_dword v53, v[28:29], off
	global_load_dword v54, v[26:27], off
	global_load_dword v55, v[32:33], off
	global_load_dword v56, v[30:31], off
	global_load_dword v57, v[36:37], off
	global_load_dword v58, v[34:35], off
	global_load_dword v59, v[40:41], off
	global_load_dword v60, v[38:39], off
	global_load_dword v61, v[44:45], off
	global_load_dword v62, v[42:43], off
	global_load_dword v63, v[48:49], off
	global_load_dword v64, v[46:47], off
	v_or_b32_e32 v16, s21, v1
	v_or_b32_e32 v14, s28, v6
	s_add_i32 s19, s19, 16
	s_add_i32 s4, s4, 16
	s_add_i32 s20, s20, -16
	v_mad_u64_u32 v[14:15], s[40:41], v14, s13, v[10:11]
	v_mad_u64_u32 v[16:17], s[40:41], v16, s13, v[10:11]
	v_or_b32_e32 v15, s29, v1
	v_or_b32_e32 v17, s30, v6
	v_or_b32_e32 v28, s31, v1
	v_or_b32_e32 v26, s34, v6
	v_or_b32_e32 v32, s35, v1
	v_or_b32_e32 v30, s39, v6
	v_or_b32_e32 v36, s42, v1
	v_or_b32_e32 v34, s43, v6
	v_or_b32_e32 v40, s44, v1
	v_or_b32_e32 v38, s45, v6
	v_or_b32_e32 v44, s46, v1
	v_or_b32_e32 v42, s47, v6
	v_or_b32_e32 v48, s48, v1
	v_or_b32_e32 v46, s49, v6
	s_cmp_lg_u32 s20, 0
	v_mad_u64_u32 v[22:23], s[28:29], v17, s13, v[10:11]
	v_mad_u64_u32 v[24:25], s[28:29], v15, s13, v[10:11]
	v_mad_u64_u32 v[26:27], s[28:29], v26, s13, v[10:11]
	v_mad_u64_u32 v[28:29], s[28:29], v28, s13, v[10:11]
	v_mad_u64_u32 v[30:31], s[28:29], v30, s13, v[10:11]
	v_mad_u64_u32 v[32:33], s[28:29], v32, s13, v[10:11]
	v_mad_u64_u32 v[34:35], s[28:29], v34, s13, v[10:11]
	v_mad_u64_u32 v[36:37], s[28:29], v36, s13, v[10:11]
	v_mad_u64_u32 v[38:39], s[28:29], v38, s13, v[10:11]
	v_mad_u64_u32 v[40:41], s[28:29], v40, s13, v[10:11]
	v_mad_u64_u32 v[42:43], s[28:29], v42, s13, v[10:11]
	v_mad_u64_u32 v[44:45], s[28:29], v44, s13, v[10:11]
	v_mad_u64_u32 v[46:47], s[28:29], v46, s13, v[10:11]
	v_mad_u64_u32 v[48:49], s[28:29], v48, s13, v[10:11]
	s_lshl_b32 s21, s4, 1
	s_lshl_b32 s28, s19, 1
	v_or_b32_e32 v80, s28, v4
	s_add_i32 s29, s21, 4
	s_add_i32 s30, s28, 4
	s_add_i32 s31, s21, 8
	s_add_i32 s34, s28, 8
	s_add_i32 s35, s21, 12
	s_add_i32 s39, s28, 12
	s_add_i32 s42, s21, 16
	s_add_i32 s43, s28, 16
	s_add_i32 s44, s21, 20
	s_add_i32 s45, s28, 20
	s_add_i32 s46, s21, 24
	s_add_i32 s47, s28, 24
	s_add_i32 s48, s21, 28
	s_add_i32 s49, s28, 28
	v_or_b32_e32 v78, s21, v5
	v_ashrrev_i32_e32 v81, 31, v80
	v_or_b32_e32 v86, s29, v5
	v_or_b32_e32 v88, s30, v4
	v_or_b32_e32 v90, s31, v5
	v_or_b32_e32 v92, s34, v4
	v_or_b32_e32 v94, s35, v5
	v_or_b32_e32 v96, s39, v4
	v_or_b32_e32 v98, s42, v5
	v_or_b32_e32 v100, s43, v4
	v_or_b32_e32 v102, s44, v5
	v_or_b32_e32 v104, s45, v4
	v_or_b32_e32 v106, s46, v5
	v_or_b32_e32 v108, s47, v4
	v_or_b32_e32 v110, s48, v5
	v_or_b32_e32 v112, s49, v4
	v_ashrrev_i32_e32 v79, 31, v78
	v_lshlrev_b64 v[80:81], 16, v[80:81]
	v_ashrrev_i32_e32 v89, 31, v88
	v_ashrrev_i32_e32 v87, 31, v86
	v_ashrrev_i32_e32 v93, 31, v92
	v_ashrrev_i32_e32 v91, 31, v90
	v_ashrrev_i32_e32 v97, 31, v96
	v_ashrrev_i32_e32 v95, 31, v94
	v_ashrrev_i32_e32 v101, 31, v100
	v_ashrrev_i32_e32 v99, 31, v98
	v_ashrrev_i32_e32 v105, 31, v104
	v_ashrrev_i32_e32 v103, 31, v102
	v_ashrrev_i32_e32 v109, 31, v108
	v_ashrrev_i32_e32 v107, 31, v106
	v_ashrrev_i32_e32 v113, 31, v112
	v_ashrrev_i32_e32 v111, 31, v110
	v_lshlrev_b64 v[78:79], 16, v[78:79]
	v_lshl_add_u64 v[80:81], v[2:3], 0, v[80:81]
	v_lshlrev_b64 v[86:87], 16, v[86:87]
	v_lshlrev_b64 v[88:89], 16, v[88:89]
	v_lshlrev_b64 v[90:91], 16, v[90:91]
	v_lshlrev_b64 v[92:93], 16, v[92:93]
	v_lshlrev_b64 v[94:95], 16, v[94:95]
	v_lshlrev_b64 v[96:97], 16, v[96:97]
	v_lshlrev_b64 v[98:99], 16, v[98:99]
	v_lshlrev_b64 v[100:101], 16, v[100:101]
	v_lshlrev_b64 v[102:103], 16, v[102:103]
	v_lshlrev_b64 v[104:105], 16, v[104:105]
	v_lshlrev_b64 v[106:107], 16, v[106:107]
	v_lshlrev_b64 v[108:109], 16, v[108:109]
	v_lshlrev_b64 v[110:111], 16, v[110:111]
	v_lshlrev_b64 v[112:113], 16, v[112:113]
	v_lshl_add_u64 v[78:79], v[2:3], 0, v[78:79]
	v_lshl_add_u64 v[88:89], v[2:3], 0, v[88:89]
	v_lshl_add_u64 v[86:87], v[2:3], 0, v[86:87]
	v_lshl_add_u64 v[92:93], v[2:3], 0, v[92:93]
	v_lshl_add_u64 v[90:91], v[2:3], 0, v[90:91]
	v_lshl_add_u64 v[96:97], v[2:3], 0, v[96:97]
	v_lshl_add_u64 v[94:95], v[2:3], 0, v[94:95]
	v_lshl_add_u64 v[100:101], v[2:3], 0, v[100:101]
	v_lshl_add_u64 v[98:99], v[2:3], 0, v[98:99]
	v_lshl_add_u64 v[104:105], v[2:3], 0, v[104:105]
	v_lshl_add_u64 v[102:103], v[2:3], 0, v[102:103]
	v_lshl_add_u64 v[108:109], v[2:3], 0, v[108:109]
	v_lshl_add_u64 v[106:107], v[2:3], 0, v[106:107]
	v_lshl_add_u64 v[112:113], v[2:3], 0, v[112:113]
	v_lshl_add_u64 v[110:111], v[2:3], 0, v[110:111]
	global_load_dword v77, v[80:81], off
	global_load_dword v114, v[78:79], off
	global_load_dword v115, v[88:89], off
	global_load_dword v116, v[86:87], off
	global_load_dword v117, v[92:93], off
	global_load_dword v118, v[90:91], off
	global_load_dword v119, v[96:97], off
	global_load_dword v120, v[94:95], off
	global_load_dword v121, v[100:101], off
	global_load_dword v122, v[98:99], off
	global_load_dword v123, v[104:105], off
	global_load_dword v124, v[102:103], off
	global_load_dword v125, v[108:109], off
	global_load_dword v126, v[106:107], off
	global_load_dword v127, v[112:113], off
	global_load_dword v128, v[110:111], off
	v_or_b32_e32 v80, s21, v1
	v_or_b32_e32 v78, s28, v6
	s_add_i32 s19, s19, 16
	s_add_i32 s4, s4, 16
	s_add_i32 s20, s20, -16
	v_mad_u64_u32 v[78:79], s[40:41], v78, s13, v[10:11]
	v_mad_u64_u32 v[80:81], s[40:41], v80, s13, v[10:11]
	v_or_b32_e32 v79, s29, v1
	v_or_b32_e32 v81, s30, v6
	v_or_b32_e32 v92, s31, v1
	v_or_b32_e32 v90, s34, v6
	v_or_b32_e32 v96, s35, v1
	v_or_b32_e32 v94, s39, v6
	v_or_b32_e32 v100, s42, v1
	v_or_b32_e32 v98, s43, v6
	v_or_b32_e32 v104, s44, v1
	v_or_b32_e32 v102, s45, v6
	v_or_b32_e32 v108, s46, v1
	v_or_b32_e32 v106, s47, v6
	v_or_b32_e32 v112, s48, v1
	v_or_b32_e32 v110, s49, v6
	s_cmp_lg_u32 s20, 0
	v_mad_u64_u32 v[86:87], s[28:29], v81, s13, v[10:11]
	v_mad_u64_u32 v[88:89], s[28:29], v79, s13, v[10:11]
	v_mad_u64_u32 v[90:91], s[28:29], v90, s13, v[10:11]
	v_mad_u64_u32 v[92:93], s[28:29], v92, s13, v[10:11]
	v_mad_u64_u32 v[94:95], s[28:29], v94, s13, v[10:11]
	v_mad_u64_u32 v[96:97], s[28:29], v96, s13, v[10:11]
	v_mad_u64_u32 v[98:99], s[28:29], v98, s13, v[10:11]
	v_mad_u64_u32 v[100:101], s[28:29], v100, s13, v[10:11]
	v_mad_u64_u32 v[102:103], s[28:29], v102, s13, v[10:11]
	v_mad_u64_u32 v[104:105], s[28:29], v104, s13, v[10:11]
	v_mad_u64_u32 v[106:107], s[28:29], v106, s13, v[10:11]
	v_mad_u64_u32 v[108:109], s[28:29], v108, s13, v[10:11]
	v_mad_u64_u32 v[110:111], s[28:29], v110, s13, v[10:11]
	v_mad_u64_u32 v[112:113], s[28:29], v112, s13, v[10:11]
	s_waitcnt vmcnt(31)
	ds_write_b32 v14, v13
	s_waitcnt vmcnt(30)
	ds_write_b32 v16, v50
	s_waitcnt vmcnt(29)
	ds_write_b32 v22, v51
	s_waitcnt vmcnt(28)
	ds_write_b32 v24, v52
	s_waitcnt vmcnt(27)
	ds_write_b32 v26, v53
	s_waitcnt vmcnt(26)
	ds_write_b32 v28, v54
	s_waitcnt vmcnt(25)
	ds_write_b32 v30, v55
	s_waitcnt vmcnt(24)
	ds_write_b32 v32, v56
	s_waitcnt vmcnt(23)
	ds_write_b32 v34, v57
	s_waitcnt vmcnt(22)
	ds_write_b32 v36, v58
	s_waitcnt vmcnt(21)
	ds_write_b32 v38, v59
	s_waitcnt vmcnt(20)
	ds_write_b32 v40, v60
	s_waitcnt vmcnt(19)
	ds_write_b32 v42, v61
	s_waitcnt vmcnt(18)
	ds_write_b32 v44, v62
	s_waitcnt vmcnt(17)
	ds_write_b32 v46, v63
	s_waitcnt vmcnt(16)
	ds_write_b32 v48, v64
	s_waitcnt vmcnt(15)
	ds_write_b32 v78, v77
	s_waitcnt vmcnt(14)
	ds_write_b32 v80, v114
	s_waitcnt vmcnt(13)
	ds_write_b32 v86, v115
	s_waitcnt vmcnt(12)
	ds_write_b32 v88, v116
	s_waitcnt vmcnt(11)
	ds_write_b32 v90, v117
	s_waitcnt vmcnt(10)
	ds_write_b32 v92, v118
	s_waitcnt vmcnt(9)
	ds_write_b32 v94, v119
	s_waitcnt vmcnt(8)
	ds_write_b32 v96, v120
	s_waitcnt vmcnt(7)
	ds_write_b32 v98, v121
	s_waitcnt vmcnt(6)
	ds_write_b32 v100, v122
	s_waitcnt vmcnt(5)
	ds_write_b32 v102, v123
	s_waitcnt vmcnt(4)
	ds_write_b32 v104, v124
	s_waitcnt vmcnt(3)
	ds_write_b32 v106, v125
	s_waitcnt vmcnt(2)
	ds_write_b32 v108, v126
	s_waitcnt vmcnt(1)
	ds_write_b32 v110, v127
	s_waitcnt vmcnt(0)
	ds_write_b32 v112, v128
	s_and_b32 s4, s18, 0xfffff800
	s_ashr_i32 s19, s23, 6
	s_addk_i32 s4, 0x800
	s_cmp_lg_u32 s19, 7
	s_cselect_b32 s4, s4, 0x3800
	s_cmp_eq_u32 s19, 2
	s_cselect_b64 s[20:21], -1, 0
	s_cmp_eq_u32 s19, 6
	s_cselect_b64 s[28:29], -1, 0
	s_or_b64 s[20:21], s[20:21], s[28:29]
	s_waitcnt lgkmcnt(0)
	s_cmp_eq_u32 s19, 1
	ds_read2_b32 v[2:3], v11 offset1:33
	ds_read2_b32 v[4:5], v11 offset0:66 offset1:99
	ds_read2_b32 v[14:15], v11 offset0:132 offset1:165
	ds_read2_b32 v[16:17], v11 offset0:198 offset1:231
	s_cselect_b64 s[30:31], -1, 0
	s_or_b64 s[28:29], s[30:31], s[28:29]
	s_and_b64 s[20:21], s[20:21], exec
	s_cselect_b32 s34, 0x80, 0
	s_and_b64 s[20:21], s[28:29], exec
	s_cselect_b32 s35, 4, 0
	s_cmp_lt_i32 s19, 7
	s_waitcnt lgkmcnt(3)
	v_cvt_pk_bf16_f32 v2, v2, v3
	s_waitcnt lgkmcnt(2)
	v_cvt_pk_bf16_f32 v3, v4, v5
	s_waitcnt lgkmcnt(1)
	v_cvt_pk_bf16_f32 v4, v14, v15
	s_waitcnt lgkmcnt(0)
	v_cvt_pk_bf16_f32 v5, v16, v17
	s_cbranch_scc1 .LBB0_31
	s_cmp_lg_u32 s19, 7
	s_mov_b64 s[20:21], -1
	s_cselect_b64 s[28:29], -1, 0
	s_cbranch_execz .LBB0_32
	s_branch .LBB0_33
